# ssd_out<false>: hoisted state fragment moved to registers of its own (it overlapped a later load's destination: write-after-read race hidden only by load latency); performance-neutral correctness fix
# speedup vs baseline: 1.0033x; 1.0033x over previous
.LBB0_1238:
	s_and_b32 s21, s54, 7
	s_lshl_b32 s0, s21, 3
	s_add_i32 s22, s0, s34
	s_lshl_b32 s14, s22, 6
	s_ashr_i32 s20, s54, 3
	s_ashr_i32 s15, s14, 31
	s_lshl_b32 s55, s20, 6
	s_lshl_b64 s[16:17], s[14:15], 1
	s_waitcnt vmcnt(8)
	v_or_b32_e32 v30, s55, v167
	v_lshl_add_u64 v[28:29], v[158:159], 0, s[16:17]
	v_mad_i64_i32 v[0:1], s[0:1], v30, s77, v[28:29]
	v_or_b32_e32 v4, 8, v30
	global_load_dwordx4 v[0:3], v[0:1], off
	v_mad_i64_i32 v[4:5], s[0:1], v4, s77, v[28:29]
	v_or_b32_e32 v8, 16, v30
	global_load_dwordx4 v[4:7], v[4:5], off
	v_mad_i64_i32 v[8:9], s[0:1], v8, s77, v[28:29]
	v_or_b32_e32 v12, 24, v30
	global_load_dwordx4 v[8:11], v[8:9], off
	v_mad_i64_i32 v[12:13], s[0:1], v12, s77, v[28:29]
	v_or_b32_e32 v16, 32, v30
	global_load_dwordx4 v[12:15], v[12:13], off
	v_mad_i64_i32 v[16:17], s[0:1], v16, s77, v[28:29]
	v_or_b32_e32 v20, 40, v30
	global_load_dwordx4 v[16:19], v[16:17], off
	v_mad_i64_i32 v[20:21], s[0:1], v20, s77, v[28:29]
	v_or_b32_e32 v24, 48, v30
	global_load_dwordx4 v[20:23], v[20:21], off
	v_mad_i64_i32 v[24:25], s[0:1], v24, s77, v[28:29]
	v_or_b32_e32 v30, 56, v30
	global_load_dwordx4 v[24:27], v[24:25], off
	v_mad_i64_i32 v[28:29], s[0:1], v30, s77, v[28:29]
	global_load_dwordx4 v[28:31], v[28:29], off
	s_lshl_b32 s0, s20, 6
	s_add_i32 s0, s0, s22
	s_lshl_b32 s0, s0, 9
	v_lshl_add_u32 v198, v161, 3, s0
	v_mov_b32_e32 v199, 0
	v_lshl_add_u64 v[198:199], s[24:25], 0, v[198:199]
	s_mov_b64 s[0:1], 0x400000
	s_nop 0
	v_lshl_add_u64 v[198:199], v[198:199], 0, s[0:1]
	global_load_dwordx2 v[198:199], v[198:199], off
	s_ashr_i32 s23, s22, 31
	s_lshl_b64 s[18:19], s[22:23], 2
	s_add_u32 s0, s26, s18
	s_addc_u32 s1, s27, s19
	v_or_b32_e32 v174, s55, v166
	v_lshlrev_b32_e32 v32, 1, v160
	s_movk_i32 s56, 0x2000
	v_mov_b32_e32 v173, v33
	s_waitcnt vmcnt(8)
	ds_write_b128 v213, v[0:3]
	s_waitcnt vmcnt(7)
	ds_write_b128 v213, v[4:7] offset:1280
	s_waitcnt vmcnt(6)
	ds_write_b128 v213, v[8:11] offset:2560
	s_waitcnt vmcnt(5)
	ds_write_b128 v213, v[12:15] offset:3840
	s_waitcnt vmcnt(4)
	ds_write_b128 v213, v[16:19] offset:5120
	s_waitcnt vmcnt(3)
	ds_write_b128 v213, v[20:23] offset:6400
	s_waitcnt vmcnt(2)
	ds_write_b128 v213, v[24:27] offset:7680
	s_waitcnt vmcnt(1)
	ds_write_b128 v213, v[28:31] offset:8960
	s_lshl_b32 s86, s21, 8
	s_ashr_i32 s21, s20, 31
	s_waitcnt vmcnt(0)
	ds_write_b32 v190, v198
	ds_write_b32 v191, v199
	v_mov_b64_e32 v[0:1], s[8:9]
	v_mad_i64_i32 v[0:1], s[0:1], v174, s77, v[0:1]
	v_lshl_add_u64 v[0:1], v[0:1], 0, s[86:87]
	v_lshl_add_u64 v[8:9], v[0:1], 0, v[32:33]
	s_mov_b64 s[0:1], 0x2800
	v_lshl_add_u64 v[74:75], v[8:9], 0, s[0:1]
	v_add_co_u32_e64 v0, s[0:1], s56, v8
	s_movk_i32 s77, 0x3000
	s_nop 0
	v_addc_co_u32_e64 v1, s[0:1], 0, v9, s[0:1]
	s_mov_b32 s0, 0x32000
	s_nop 0
	v_add_co_u32_e64 v30, s[0:1], s0, v8
	global_load_dwordx4 v[4:7], v[0:1], off offset:2048
	s_nop 0
	global_load_dwordx4 v[0:3], v[74:75], off offset:64
	global_load_dwordx4 v[70:73], v[74:75], off offset:128
	global_load_dwordx4 v[66:69], v[74:75], off offset:192
	v_addc_co_u32_e64 v31, s[0:1], 0, v9, s[0:1]
	s_mov_b32 s0, 0x62000
	s_nop 0
	v_add_co_u32_e64 v88, s[0:1], s0, v8
	global_load_dwordx4 v[62:65], v[30:31], off offset:2048
	global_load_dwordx4 v[58:61], v[30:31], off offset:2112
	global_load_dwordx4 v[54:57], v[30:31], off offset:2176
	global_load_dwordx4 v[50:53], v[30:31], off offset:2240
	v_addc_co_u32_e64 v89, s[0:1], 0, v9, s[0:1]
	s_mov_b32 s0, 0x92000
	s_nop 0
	v_add_co_u32_e64 v86, s[0:1], s0, v8
	global_load_dwordx4 v[46:49], v[88:89], off offset:2048
	global_load_dwordx4 v[42:45], v[88:89], off offset:2112
	global_load_dwordx4 v[38:41], v[88:89], off offset:2176
	global_load_dwordx4 v[24:27], v[88:89], off offset:2240
	v_addc_co_u32_e64 v87, s[0:1], 0, v9, s[0:1]
	global_load_dwordx4 v[20:23], v[86:87], off offset:2048
	global_load_dwordx4 v[16:19], v[86:87], off offset:2112
	global_load_dwordx4 v[8:11], v[86:87], off offset:2176
	global_load_dwordx4 v[12:15], v[86:87], off offset:2240
	s_waitcnt lgkmcnt(0)
	ds_read2_b32 v[102:103], v192 offset1:16
	ds_read2_b32 v[28:29], v192 offset0:32 offset1:48
	global_load_dwordx4 v[82:85], v[74:75], off offset:-2048
	global_load_dwordx4 v[92:95], v[74:75], off offset:-1984
	global_load_dwordx4 v[96:99], v[74:75], off offset:-1920
	global_load_dwordx4 v[104:107], v[74:75], off offset:-1856
	s_lshl_b32 s0, s20, 12
	s_lshl_b32 s1, s22, 6
	s_add_i32 s0, s0, s1
	v_or_b32_e32 v200, s0, v166
	v_mov_b32_e32 v201, 0
	v_lshlrev_b64 v[200:201], 8, v[200:201]
	v_lshl_add_u64 v[200:201], v[164:165], 0, v[200:201]
	global_load_dwordx4 v[144:147], v[200:201], off
	global_load_dwordx4 v[148:151], v[200:201], off offset:64
	global_load_dwordx4 v[152:155], v[200:201], off offset:128
	global_load_dwordx4 v[222:225], v[200:201], off offset:192
	s_waitcnt vmcnt(7)
	v_mfma_f32_16x16x32_bf16 v[74:77], v[82:85], v[4:7], 0
	ds_read_b64 v[100:101], v193
	ds_read_b32 v32, v195
	ds_read_b32 v90, v196
	ds_read_b32 v118, v197
	ds_read_b32 v91, v208
	s_mov_b32 s0, 0x5040100
	s_waitcnt vmcnt(6)
	v_mfma_f32_16x16x32_bf16 v[74:77], v[92:95], v[0:3], v[74:77]
	s_waitcnt vmcnt(5)
	v_mfma_f32_16x16x32_bf16 v[74:77], v[96:99], v[70:73], v[74:77]
	v_mfma_f32_16x16x32_bf16 v[108:111], v[82:85], v[62:65], 0
	s_waitcnt vmcnt(4)
	v_mfma_f32_16x16x32_bf16 v[78:81], v[104:107], v[66:69], v[74:77]
	s_waitcnt lgkmcnt(4)
	s_nop 3
	v_sub_f32_e32 v76, v103, v100
	v_min_f32_e32 v76, 0, v76
	v_mfma_f32_16x16x32_bf16 v[108:111], v[92:95], v[58:61], v[108:111]
	v_mul_f32_e32 v76, 0x3fb8aa3b, v76
	v_exp_f32_e32 v114, v76
	v_sub_f32_e32 v76, v103, v101
	v_min_f32_e32 v76, 0, v76
	v_mul_f32_e32 v76, 0x3fb8aa3b, v76
	v_mfma_f32_16x16x32_bf16 v[108:111], v[96:99], v[54:57], v[108:111]
	v_exp_f32_e32 v115, v76
	s_waitcnt lgkmcnt(3)
	v_sub_f32_e32 v76, v103, v32
	s_waitcnt lgkmcnt(1)
	v_sub_f32_e32 v77, v103, v118
	v_min_f32_e32 v76, 0, v76
	v_min_f32_e32 v77, 0, v77
	v_mul_f32_e32 v76, 0x3fb8aa3b, v76
	v_mul_f32_e32 v77, 0x3fb8aa3b, v77
	v_exp_f32_e32 v76, v76
	v_exp_f32_e32 v77, v77
	v_mfma_f32_16x16x32_bf16 v[108:111], v[104:107], v[50:53], v[108:111]
	v_sub_f32_e32 v74, v102, v100
	v_min_f32_e32 v74, 0, v74
	v_mul_f32_e32 v74, 0x3fb8aa3b, v74
	s_waitcnt lgkmcnt(0)
	v_pk_mul_f32 v[76:77], v[90:91], v[76:77]
	v_exp_f32_e32 v119, v74
	v_sub_f32_e32 v74, v102, v101
	s_nop 0
	v_pk_mul_f32 v[76:77], v[76:77], v[110:111]
	v_mfma_f32_16x16x32_bf16 v[110:113], v[82:85], v[46:49], 0
	v_min_f32_e32 v74, 0, v74
	v_mul_f32_e32 v74, 0x3fb8aa3b, v74
	v_exp_f32_e32 v120, v74
	v_mfma_f32_16x16x32_bf16 v[82:85], v[82:85], v[20:23], 0
	v_sub_f32_e32 v74, v102, v32
	v_sub_f32_e32 v75, v102, v118
	v_min_f32_e32 v74, 0, v74
	v_min_f32_e32 v75, 0, v75
	v_mfma_f32_16x16x32_bf16 v[82:85], v[92:95], v[16:19], v[82:85]
	v_mul_f32_e32 v74, 0x3fb8aa3b, v74
	v_mul_f32_e32 v75, 0x3fb8aa3b, v75
	v_exp_f32_e32 v74, v74
	v_exp_f32_e32 v75, v75
	v_mfma_f32_16x16x32_bf16 v[82:85], v[96:99], v[8:11], v[82:85]
	v_mul_f32_e64 v74, v90, v74
	v_mul_f32_e64 v75, v91, v75
	v_mfma_f32_16x16x32_bf16 v[110:113], v[92:95], v[42:45], v[110:113]
	v_mul_f32_e64 v74, v74, v80
	v_mul_f32_e64 v75, v75, v81
	v_sub_f32_e32 v80, v28, v100
	v_min_f32_e32 v80, 0, v80
	v_mfma_f32_16x16x32_bf16 v[92:95], v[104:107], v[12:15], v[82:85]
	v_mul_f32_e32 v80, 0x3fb8aa3b, v80
	v_exp_f32_e32 v116, v80
	v_sub_f32_e32 v80, v28, v101
	v_sub_f32_e32 v82, v29, v100
	v_sub_f32_e32 v83, v29, v101
	v_min_f32_e32 v82, 0, v82
	v_min_f32_e32 v83, 0, v83
	v_mfma_f32_16x16x32_bf16 v[110:113], v[96:99], v[38:41], v[110:113]
	v_mul_f32_e32 v82, 0x3fb8aa3b, v82
	v_mul_f32_e32 v83, 0x3fb8aa3b, v83
	ds_read_b64 v[96:97], v194
	v_min_f32_e32 v80, 0, v80
	v_exp_f32_e32 v82, v82
	v_exp_f32_e32 v83, v83
	v_mul_f32_e32 v80, 0x3fb8aa3b, v80
	v_exp_f32_e32 v117, v80
	v_sub_f32_e32 v80, v28, v32
	v_sub_f32_e32 v32, v29, v32
	v_min_f32_e32 v32, 0, v32
	s_waitcnt lgkmcnt(0)
	v_pk_mul_f32 v[82:83], v[96:97], v[82:83]
	v_mul_f32_e32 v32, 0x3fb8aa3b, v32
	v_sub_f32_e32 v81, v28, v118
	v_pk_mul_f32 v[82:83], v[82:83], v[92:93]
	v_exp_f32_e32 v92, v32
	v_sub_f32_e32 v32, v29, v118
	v_min_f32_e32 v80, 0, v80
	v_min_f32_e32 v81, 0, v81
	v_min_f32_e32 v32, 0, v32
	v_mul_f32_e32 v80, 0x3fb8aa3b, v80
	v_mul_f32_e32 v81, 0x3fb8aa3b, v81
	v_mul_f32_e32 v84, v96, v119
	v_mul_f32_e32 v32, 0x3fb8aa3b, v32
	v_exp_f32_e32 v80, v80
	v_exp_f32_e32 v81, v81
	v_mul_f32_e32 v78, v84, v78
	v_exp_f32_e32 v93, v32
	v_mfma_f32_16x16x32_bf16 v[110:113], v[104:107], v[24:27], v[110:113]
	v_cndmask_b32_e64 v126, v78, 0, s[46:47]
	v_mul_f32_e32 v78, v97, v120
	v_mul_f32_e32 v78, v78, v79
	v_cndmask_b32_e64 v127, 0, v78, s[48:49]
	v_pk_mul_f32 v[78:79], v[96:97], v[114:115]
	v_pk_mul_f32 v[80:81], v[90:91], v[80:81]
	v_pk_mul_f32 v[84:85], v[78:79], v[108:109]
	v_pk_mul_f32 v[78:79], v[96:97], v[116:117]
	v_pk_mul_f32 v[90:91], v[90:91], v[92:93]
	v_pk_mul_f32 v[78:79], v[78:79], v[110:111]
	v_pk_mul_f32 v[90:91], v[90:91], v[94:95]
	global_load_dwordx4 v[92:95], v[30:31], off
	global_load_dwordx4 v[96:99], v[30:31], off offset:64
	global_load_dwordx4 v[104:107], v[30:31], off offset:128
	global_load_dwordx4 v[108:111], v[30:31], off offset:192
	v_pk_mul_f32 v[80:81], v[80:81], v[112:113]
	ds_read_b128 v[112:115], v193 offset:64
	s_waitcnt vmcnt(3)
	v_mfma_f32_16x16x32_bf16 v[116:119], v[92:95], v[62:65], 0
	s_waitcnt lgkmcnt(0)
	v_sub_f32_e32 v30, v103, v112
	v_min_f32_e32 v30, 0, v30
	v_mul_f32_e32 v30, 0x3fb8aa3b, v30
	v_mfma_f32_16x16x32_bf16 v[120:123], v[92:95], v[46:49], 0
	v_exp_f32_e32 v32, v30
	v_sub_f32_e32 v30, v103, v113
	v_min_f32_e32 v30, 0, v30
	v_mfma_f32_16x16x32_bf16 v[92:95], v[92:95], v[20:23], 0
	v_mul_f32_e32 v30, 0x3fb8aa3b, v30
	v_exp_f32_e32 v128, v30
	v_sub_f32_e32 v100, v28, v112
	s_waitcnt vmcnt(2)
	v_mfma_f32_16x16x32_bf16 v[116:119], v[96:99], v[58:61], v[116:119]
	v_sub_f32_e32 v101, v28, v113
	v_min_f32_e32 v100, 0, v100
	v_min_f32_e32 v101, 0, v101
	v_mfma_f32_16x16x32_bf16 v[120:123], v[96:99], v[42:45], v[120:123]
	v_mul_f32_e32 v100, 0x3fb8aa3b, v100
	v_mul_f32_e32 v101, 0x3fb8aa3b, v101
	v_exp_f32_e32 v100, v100
	v_mfma_f32_16x16x32_bf16 v[92:95], v[96:99], v[16:19], v[92:95]
	v_sub_f32_e32 v96, v29, v112
	v_min_f32_e32 v96, 0, v96
	v_mul_f32_e32 v96, 0x3fb8aa3b, v96
	s_waitcnt vmcnt(1)
	v_mfma_f32_16x16x32_bf16 v[116:119], v[104:107], v[54:57], v[116:119]
	v_exp_f32_e32 v101, v101
	v_sub_f32_e32 v30, v103, v114
	v_sub_f32_e32 v31, v103, v115
	v_mfma_f32_16x16x32_bf16 v[120:123], v[104:107], v[38:41], v[120:123]
	v_min_f32_e32 v30, 0, v30
	v_min_f32_e32 v31, 0, v31
	v_sub_f32_e32 v124, v28, v114
	v_mfma_f32_16x16x32_bf16 v[92:95], v[104:107], v[8:11], v[92:95]
	v_exp_f32_e32 v104, v96
	v_sub_f32_e32 v96, v29, v113
	v_min_f32_e32 v96, 0, v96
	v_mul_f32_e32 v96, 0x3fb8aa3b, v96
	v_exp_f32_e32 v105, v96
	ds_read_b128 v[96:99], v194 offset:64
	s_waitcnt vmcnt(0)
	v_mfma_f32_16x16x32_bf16 v[116:119], v[108:111], v[50:53], v[116:119]
	v_sub_f32_e32 v125, v28, v115
	v_mul_f32_e32 v30, 0x3fb8aa3b, v30
	v_mul_f32_e32 v31, 0x3fb8aa3b, v31
	s_waitcnt lgkmcnt(0)
	v_mul_f32_e32 v32, v96, v32
	v_mfma_f32_16x16x32_bf16 v[120:123], v[108:111], v[24:27], v[120:123]
	s_nop 1
	v_mul_f32_e32 v32, v32, v116
	v_pk_mul_f32 v[100:101], v[96:97], v[100:101]
	v_min_f32_e32 v124, 0, v124
	v_mfma_f32_16x16x32_bf16 v[92:95], v[108:111], v[12:15], v[92:95]
	v_cndmask_b32_e64 v108, v32, 0, s[46:47]
	v_mul_f32_e32 v32, v97, v128
	v_mul_f32_e32 v32, v32, v117
	v_cndmask_b32_e64 v109, 0, v32, s[48:49]
	v_sub_f32_e32 v32, v29, v114
	v_min_f32_e32 v32, 0, v32
	v_pk_mul_f32 v[96:97], v[96:97], v[104:105]
	v_mul_f32_e32 v32, 0x3fb8aa3b, v32
	v_min_f32_e32 v125, 0, v125
	v_pk_mul_f32 v[92:93], v[96:97], v[92:93]
	v_exp_f32_e32 v96, v32
	v_sub_f32_e32 v32, v29, v115
	v_exp_f32_e32 v30, v30
	v_exp_f32_e32 v31, v31
	v_mul_f32_e32 v124, 0x3fb8aa3b, v124
	v_mul_f32_e32 v125, 0x3fb8aa3b, v125
	v_min_f32_e32 v32, 0, v32
	v_exp_f32_e32 v124, v124
	v_exp_f32_e32 v125, v125
	v_mul_f32_e32 v32, 0x3fb8aa3b, v32
	v_exp_f32_e32 v97, v32
	v_pk_mul_f32 v[30:31], v[98:99], v[30:31]
	v_pk_mul_f32 v[100:101], v[100:101], v[120:121]
	v_pk_mul_f32 v[104:105], v[30:31], v[118:119]
	v_pk_mul_f32 v[30:31], v[98:99], v[124:125]
	v_cvt_pk_bf16_f32 v78, v78, v79
	v_pk_mul_f32 v[106:107], v[30:31], v[122:123]
	v_pk_mul_f32 v[30:31], v[98:99], v[96:97]
	v_cvt_pk_bf16_f32 v79, v80, v81
	v_pk_mul_f32 v[94:95], v[30:31], v[94:95]
	v_cvt_pk_bf16_f32 v31, v74, v75
	v_cvt_pk_bf16_f32 v75, v76, v77
	v_cvt_pk_bf16_f32 v77, v104, v105
	v_cvt_pk_bf16_f32 v74, v84, v85
	v_cndmask_b32_e64 v84, v77, 0, s[52:53]
	v_lshrrev_b32_e32 v77, 16, v77
	v_cndmask_b32_e64 v77, v77, 0, s[50:51]
	v_perm_b32 v77, v77, v84, s0
	v_cvt_pk_bf16_f32 v80, v100, v101
	v_cvt_pk_bf16_f32 v81, v106, v107
	v_cvt_pk_bf16_f32 v82, v82, v83
	v_cvt_pk_bf16_f32 v83, v90, v91
	v_cvt_pk_bf16_f32 v84, v92, v93
	v_cvt_pk_bf16_f32 v85, v94, v95
	global_load_dwordx4 v[90:93], v[88:89], off
	global_load_dwordx4 v[94:97], v[88:89], off offset:64
	global_load_dwordx4 v[98:101], v[88:89], off offset:128
	global_load_dwordx4 v[104:107], v[88:89], off offset:192
	v_cvt_pk_bf16_f32 v76, v108, v109
	ds_read_b128 v[108:111], v193 offset:128
	s_waitcnt vmcnt(3)
	v_mfma_f32_16x16x32_bf16 v[112:115], v[90:93], v[46:49], 0
	s_waitcnt lgkmcnt(0)
	v_sub_f32_e32 v88, v28, v108
	v_min_f32_e32 v88, 0, v88
	v_mul_f32_e32 v88, 0x3fb8aa3b, v88
	v_exp_f32_e32 v118, v88
	v_sub_f32_e32 v88, v28, v109
	v_min_f32_e32 v88, 0, v88
	v_mul_f32_e32 v88, 0x3fb8aa3b, v88
	v_exp_f32_e32 v119, v88
	v_sub_f32_e32 v88, v28, v110
	v_min_f32_e32 v88, 0, v88
	v_mul_f32_e32 v88, 0x3fb8aa3b, v88
	v_exp_f32_e32 v116, v88
	v_sub_f32_e32 v88, v28, v111
	v_min_f32_e32 v88, 0, v88
	v_mul_f32_e32 v88, 0x3fb8aa3b, v88
	v_exp_f32_e32 v117, v88
	v_mfma_f32_16x16x32_bf16 v[88:91], v[90:93], v[20:23], 0
	v_cndmask_b32_e64 v32, v31, 0, s[52:53]
	v_lshrrev_b32_e32 v31, 16, v31
	v_cndmask_b32_e64 v31, v31, 0, s[50:51]
	s_waitcnt vmcnt(2)
	v_mfma_f32_16x16x32_bf16 v[88:91], v[94:97], v[16:19], v[88:91]
	v_perm_b32 v31, v31, v32, s0
	v_cvt_pk_bf16_f32 v30, v126, v127
	v_mul_f32_e32 v28, 0x3fb8aa3b, v28
	s_waitcnt vmcnt(1)
	v_mfma_f32_16x16x32_bf16 v[88:91], v[98:101], v[8:11], v[88:91]
	v_exp_f32_e32 v178, v28
	v_mul_f32_e32 v28, 0x3fb8aa3b, v29
	v_exp_f32_e32 v28, v28
	s_waitcnt vmcnt(0)
	v_mfma_f32_16x16x32_bf16 v[90:93], v[104:107], v[12:15], v[88:91]
	v_mov_b32_e32 v32, v33
	s_nop 1
	v_sub_f32_e32 v88, v29, v108
	v_sub_f32_e32 v89, v29, v109
	v_mfma_f32_16x16x32_bf16 v[112:115], v[94:97], v[42:45], v[112:115]
	v_min_f32_e32 v88, 0, v88
	v_min_f32_e32 v89, 0, v89
	v_mul_f32_e32 v88, 0x3fb8aa3b, v88
	v_mul_f32_e32 v89, 0x3fb8aa3b, v89
	ds_read_b128 v[94:97], v194 offset:128
	v_exp_f32_e32 v88, v88
	v_exp_f32_e32 v89, v89
	v_mfma_f32_16x16x32_bf16 v[112:115], v[98:101], v[38:41], v[112:115]
	s_waitcnt lgkmcnt(0)
	v_mul_f32_e32 v98, v94, v118
	v_pk_mul_f32 v[88:89], v[94:95], v[88:89]
	v_mfma_f32_16x16x32_bf16 v[112:115], v[104:107], v[24:27], v[112:115]
	v_mul_f32_e64 v90, v88, v90
	v_mul_f32_e64 v91, v89, v91
	v_sub_f32_e32 v88, v29, v110
	v_min_f32_e32 v88, 0, v88
	v_mul_f32_e32 v88, 0x3fb8aa3b, v88
	v_exp_f32_e32 v94, v88
	v_sub_f32_e32 v88, v29, v111
	v_min_f32_e32 v88, 0, v88
	v_mul_f32_e32 v98, v98, v112
	v_mul_f32_e32 v88, 0x3fb8aa3b, v88
	v_cndmask_b32_e64 v120, v98, 0, s[46:47]
	v_mul_f32_e32 v98, v95, v119
	v_exp_f32_e32 v95, v88
	v_mul_f32_e32 v98, v98, v113
	v_cndmask_b32_e64 v121, 0, v98, s[48:49]
	v_pk_mul_f32 v[88:89], v[96:97], v[116:117]
	v_pk_mul_f32 v[94:95], v[96:97], v[94:95]
	v_pk_mul_f32 v[88:89], v[88:89], v[114:115]
	v_pk_mul_f32 v[92:93], v[94:95], v[92:93]
	global_load_dwordx4 v[94:97], v[86:87], off
	global_load_dwordx4 v[98:101], v[86:87], off offset:64
	global_load_dwordx4 v[104:107], v[86:87], off offset:128
	global_load_dwordx4 v[108:111], v[86:87], off offset:192
	s_waitcnt vmcnt(3)
	v_mfma_f32_16x16x32_bf16 v[94:97], v[94:97], v[20:23], 0
	ds_read_b128 v[112:115], v193 offset:192
	ds_read_b128 v[116:119], v194 offset:192
	v_cvt_pk_bf16_f32 v90, v90, v91
	v_cvt_pk_bf16_f32 v91, v92, v93
	s_waitcnt vmcnt(2)
	v_mfma_f32_16x16x32_bf16 v[94:97], v[98:101], v[16:19], v[94:97]
	s_waitcnt lgkmcnt(1)
	v_sub_f32_e32 v86, v29, v112
	v_min_f32_e32 v86, 0, v86
	v_mul_f32_e32 v86, 0x3fb8aa3b, v86
	s_waitcnt vmcnt(1)
	v_mfma_f32_16x16x32_bf16 v[94:97], v[104:107], v[8:11], v[94:97]
	v_exp_f32_e32 v86, v86
	v_sub_f32_e32 v87, v29, v115
	v_min_f32_e32 v87, 0, v87
	s_waitcnt vmcnt(0)
	v_mfma_f32_16x16x32_bf16 v[94:97], v[108:111], v[12:15], v[94:97]
	s_waitcnt lgkmcnt(0)
	v_mul_f32_e32 v86, v116, v86
	v_mul_f32_e32 v87, 0x3fb8aa3b, v87
	v_exp_f32_e32 v87, v87
	s_nop 3
	v_mul_f32_e32 v86, v86, v94
	v_cndmask_b32_e64 v98, v86, 0, s[46:47]
	v_sub_f32_e32 v86, v29, v113
	v_min_f32_e32 v86, 0, v86
	v_mul_f32_e32 v86, 0x3fb8aa3b, v86
	v_exp_f32_e32 v86, v86
	s_nop 0
	v_mul_f32_e32 v86, v117, v86
	v_mul_f32_e32 v86, v86, v95
	v_cndmask_b32_e64 v99, 0, v86, s[48:49]
	v_sub_f32_e32 v86, v29, v114
	v_min_f32_e32 v86, 0, v86
	v_mul_f32_e32 v86, 0x3fb8aa3b, v86
	v_exp_f32_e32 v86, v86
	v_cvt_pk_bf16_f32 v92, v98, v99
	v_mul_f32_e32 v98, 0x3fb8aa3b, v102
	v_mul_f32_e32 v102, 0x3fb8aa3b, v103
	v_pk_mul_f32 v[86:87], v[118:119], v[86:87]
	v_exp_f32_e32 v180, v98
	v_pk_mul_f32 v[94:95], v[86:87], v[96:97]
	v_cvt_pk_bf16_f32 v87, v88, v89
	v_cvt_pk_bf16_f32 v93, v94, v95
	v_cndmask_b32_e64 v88, v87, 0, s[52:53]
	v_lshrrev_b32_e32 v87, 16, v87
	v_cndmask_b32_e64 v94, v93, 0, s[52:53]
	v_lshrrev_b32_e32 v93, 16, v93
	v_cndmask_b32_e64 v87, v87, 0, s[50:51]
	v_cndmask_b32_e64 v93, v93, 0, s[50:51]
	v_perm_b32 v87, v87, v88, s0
	v_perm_b32 v93, v93, v94, s0
	s_lshl_b64 s[0:1], s[20:21], 12
	s_lshl_b64 s[20:21], s[22:23], 6
	s_add_u32 s0, s20, s0
	s_addc_u32 s1, s21, s1
	v_mov_b32_e32 v95, s1
	v_or_b32_e32 v94, s0, v166
	v_lshlrev_b64 v[94:95], 8, v[94:95]
	v_lshl_add_u64 v[142:143], v[164:165], 0, v[94:95]
	v_cvt_pk_bf16_f32 v86, v120, v121
	s_waitcnt vmcnt(3)
	v_mfma_f32_16x16x32_bf16 v[94:97], v[144:147], v[4:7], 0
	v_exp_f32_e32 v176, v102
	s_movk_i32 s0, 0x1000
	v_mfma_f32_16x16x32_bf16 v[98:101], v[144:147], v[62:65], 0
	v_mov_b32_e32 v88, v33
	v_mov_b32_e32 v89, v33
	v_mfma_f32_16x16x32_bf16 v[102:105], v[144:147], v[46:49], 0
	v_mfma_f32_16x16x32_bf16 v[106:109], v[144:147], v[20:23], 0
	s_waitcnt vmcnt(2)
	v_mfma_f32_16x16x32_bf16 v[94:97], v[148:151], v[0:3], v[94:97]
	v_mfma_f32_16x16x32_bf16 v[98:101], v[148:151], v[58:61], v[98:101]
	v_mfma_f32_16x16x32_bf16 v[102:105], v[148:151], v[42:45], v[102:105]
	v_mfma_f32_16x16x32_bf16 v[106:109], v[148:151], v[16:19], v[106:109]
	v_add_co_u32_e64 v110, s[0:1], s0, v142
	s_nop 1
	v_addc_co_u32_e64 v111, s[0:1], 0, v143, s[0:1]
	v_add_co_u32_e64 v126, s[0:1], s56, v142
	s_waitcnt vmcnt(1)
	v_mfma_f32_16x16x32_bf16 v[94:97], v[152:155], v[70:73], v[94:97]
	v_addc_co_u32_e64 v127, s[0:1], 0, v143, s[0:1]
	global_load_dwordx4 v[122:125], v[126:127], off offset:-4096
	global_load_dwordx4 v[128:131], v[110:111], off offset:64
	global_load_dwordx4 v[132:135], v[110:111], off offset:128
	global_load_dwordx4 v[136:139], v[110:111], off offset:192
	v_mfma_f32_16x16x32_bf16 v[98:101], v[152:155], v[54:57], v[98:101]
	v_mfma_f32_16x16x32_bf16 v[102:105], v[152:155], v[38:41], v[102:105]
	v_mfma_f32_16x16x32_bf16 v[106:109], v[152:155], v[8:11], v[106:109]
	s_waitcnt vmcnt(4)
	v_mfma_f32_16x16x32_bf16 v[94:97], v[222:225], v[66:69], v[94:97]
	v_mfma_f32_16x16x32_bf16 v[98:101], v[222:225], v[50:53], v[98:101]
	v_mfma_f32_16x16x32_bf16 v[102:105], v[222:225], v[24:27], v[102:105]
	s_nop 5
	v_mul_f32_e64 v96, v180, v96
	v_mul_f32_e64 v97, v180, v97
	v_pk_mul_f32 v[94:95], v[180:181], v[94:95] op_sel_hi:[0,1]
	v_mfma_f32_16x16x32_bf16 v[106:109], v[222:225], v[12:15], v[106:109]
	s_waitcnt vmcnt(3)
	v_mfma_f32_16x16x32_bf16 v[110:113], v[122:125], v[4:7], 0
	v_mul_f32_e64 v104, v178, v104
	v_mul_f32_e64 v105, v178, v105
	v_pk_mul_f32 v[102:103], v[178:179], v[102:103] op_sel_hi:[0,1]
	s_nop 2
	v_pk_mul_f32 v[108:109], v[28:29], v[108:109] op_sel_hi:[0,1]
	v_mfma_f32_16x16x32_bf16 v[114:117], v[122:125], v[62:65], 0
	v_mul_f32_e64 v106, v28, v106
	v_mul_f32_e64 v107, v28, v107
	v_mfma_f32_16x16x32_bf16 v[118:121], v[122:125], v[46:49], 0
	v_mfma_f32_16x16x32_bf16 v[122:125], v[122:125], v[20:23], 0
	s_waitcnt vmcnt(2)
	v_mfma_f32_16x16x32_bf16 v[110:113], v[128:131], v[0:3], v[110:113]
	v_mfma_f32_16x16x32_bf16 v[114:117], v[128:131], v[58:61], v[114:117]
	v_mfma_f32_16x16x32_bf16 v[118:121], v[128:131], v[42:45], v[118:121]
	v_mfma_f32_16x16x32_bf16 v[122:125], v[128:131], v[16:19], v[122:125]
	s_waitcnt vmcnt(1)
	v_mfma_f32_16x16x32_bf16 v[110:113], v[132:135], v[70:73], v[110:113]
	v_mfma_f32_16x16x32_bf16 v[114:117], v[132:135], v[54:57], v[114:117]
	v_mfma_f32_16x16x32_bf16 v[118:121], v[132:135], v[38:41], v[118:121]
	v_mfma_f32_16x16x32_bf16 v[122:125], v[132:135], v[8:11], v[122:125]
	s_waitcnt vmcnt(0)
	v_mfma_f32_16x16x32_bf16 v[110:113], v[136:139], v[66:69], v[110:113]
	v_mfma_f32_16x16x32_bf16 v[114:117], v[136:139], v[50:53], v[114:117]
	v_mfma_f32_16x16x32_bf16 v[118:121], v[136:139], v[24:27], v[118:121]
	s_nop 5
	v_mul_f32_e64 v112, v180, v112
	v_mul_f32_e64 v113, v180, v113
	v_pk_mul_f32 v[110:111], v[180:181], v[110:111] op_sel_hi:[0,1]
	v_pk_mul_f32 v[116:117], v[176:177], v[116:117] op_sel_hi:[0,1]
	v_mfma_f32_16x16x32_bf16 v[122:125], v[136:139], v[12:15], v[122:125]
	global_load_dwordx4 v[138:141], v[126:127], off
	global_load_dwordx4 v[144:147], v[126:127], off offset:64
	global_load_dwordx4 v[148:151], v[126:127], off offset:128
	global_load_dwordx4 v[152:155], v[126:127], off offset:192
	v_pk_mul_f32 v[114:115], v[176:177], v[114:115] op_sel_hi:[0,1]
	s_waitcnt vmcnt(3)
	v_mfma_f32_16x16x32_bf16 v[126:129], v[138:141], v[4:7], 0
	v_mul_f32_e64 v120, v178, v120
	v_mul_f32_e64 v121, v178, v121
	v_pk_mul_f32 v[118:119], v[178:179], v[118:119] op_sel_hi:[0,1]
	v_pk_mul_f32 v[124:125], v[28:29], v[124:125] op_sel_hi:[0,1]
	v_mfma_f32_16x16x32_bf16 v[130:133], v[138:141], v[62:65], 0
	v_mul_f32_e64 v122, v28, v122
	v_mul_f32_e64 v123, v28, v123
	v_mfma_f32_16x16x32_bf16 v[134:137], v[138:141], v[46:49], 0
	v_mfma_f32_16x16x32_bf16 v[138:141], v[138:141], v[20:23], 0
	s_waitcnt vmcnt(2)
	v_mfma_f32_16x16x32_bf16 v[126:129], v[144:147], v[0:3], v[126:129]
	v_mfma_f32_16x16x32_bf16 v[130:133], v[144:147], v[58:61], v[130:133]
	v_mfma_f32_16x16x32_bf16 v[134:137], v[144:147], v[42:45], v[134:137]
	v_mfma_f32_16x16x32_bf16 v[138:141], v[144:147], v[16:19], v[138:141]
	s_waitcnt vmcnt(1)
	v_mfma_f32_16x16x32_bf16 v[126:129], v[148:151], v[70:73], v[126:129]
	v_mfma_f32_16x16x32_bf16 v[130:133], v[148:151], v[54:57], v[130:133]
	v_mfma_f32_16x16x32_bf16 v[134:137], v[148:151], v[38:41], v[134:137]
	v_mfma_f32_16x16x32_bf16 v[138:141], v[148:151], v[8:11], v[138:141]
	s_waitcnt vmcnt(0)
	v_mfma_f32_16x16x32_bf16 v[126:129], v[152:155], v[66:69], v[126:129]
	v_mfma_f32_16x16x32_bf16 v[130:133], v[152:155], v[50:53], v[130:133]
	v_mfma_f32_16x16x32_bf16 v[134:137], v[152:155], v[24:27], v[134:137]
	s_nop 5
	v_mul_f32_e64 v128, v180, v128
	v_mul_f32_e64 v129, v180, v129
	v_pk_mul_f32 v[126:127], v[180:181], v[126:127] op_sel_hi:[0,1]
	v_pk_mul_f32 v[132:133], v[176:177], v[132:133] op_sel_hi:[0,1]
	v_mfma_f32_16x16x32_bf16 v[138:141], v[152:155], v[12:15], v[138:141]
	v_add_co_u32_e64 v154, s[0:1], s77, v142
	v_pk_mul_f32 v[130:131], v[176:177], v[130:131] op_sel_hi:[0,1]
	s_nop 0
	v_addc_co_u32_e64 v155, s[0:1], 0, v143, s[0:1]
	global_load_dwordx4 v[142:145], v[154:155], off
	global_load_dwordx4 v[146:149], v[154:155], off offset:64
	global_load_dwordx4 v[150:153], v[154:155], off offset:128
	s_nop 0
	global_load_dwordx4 v[154:157], v[154:155], off offset:192
	s_waitcnt vmcnt(3)
	v_mfma_f32_16x16x32_bf16 v[4:7], v[142:145], v[4:7], 0
	v_mul_f32_e64 v136, v178, v136
	v_mul_f32_e64 v137, v178, v137
	v_pk_mul_f32 v[134:135], v[178:179], v[134:135] op_sel_hi:[0,1]
	s_waitcnt vmcnt(2)
	v_mfma_f32_16x16x32_bf16 v[0:3], v[146:149], v[0:3], v[4:7]
	v_mul_f32_e64 v140, v28, v140
	v_mul_f32_e64 v141, v28, v141
	v_pk_mul_f32 v[138:139], v[28:29], v[138:139] op_sel_hi:[0,1]
	s_add_u32 s0, s30, s18
	s_waitcnt vmcnt(1)
	v_mfma_f32_16x16x32_bf16 v[0:3], v[150:153], v[70:73], v[0:3]
	s_addc_u32 s1, s31, s19
	s_waitcnt vmcnt(0)
	v_mfma_f32_16x16x32_bf16 v[0:3], v[154:157], v[66:69], v[0:3]
	s_nop 7
	v_pk_mul_f32 v[68:69], v[180:181], v[2:3] op_sel_hi:[0,1]
	v_pk_mul_f32 v[66:67], v[180:181], v[0:1] op_sel_hi:[0,1]
	v_mfma_f32_16x16x32_bf16 v[0:3], v[142:145], v[62:65], 0
	v_mfma_f32_16x16x32_bf16 v[0:3], v[146:149], v[58:61], v[0:3]
	v_mfma_f32_16x16x32_bf16 v[0:3], v[150:153], v[54:57], v[0:3]
	v_mfma_f32_16x16x32_bf16 v[0:3], v[154:157], v[50:53], v[0:3]
	s_nop 7
	v_pk_mul_f32 v[72:73], v[176:177], v[2:3] op_sel_hi:[0,1]
	v_pk_mul_f32 v[70:71], v[176:177], v[0:1] op_sel_hi:[0,1]
	v_mfma_f32_16x16x32_bf16 v[0:3], v[142:145], v[46:49], 0
	v_mfma_f32_16x16x32_bf16 v[0:3], v[146:149], v[42:45], v[0:3]
	v_mfma_f32_16x16x32_bf16 v[0:3], v[150:153], v[38:41], v[0:3]
	v_mfma_f32_16x16x32_bf16 v[0:3], v[154:157], v[24:27], v[0:3]
	s_nop 7
	v_pk_mul_f32 v[26:27], v[178:179], v[2:3] op_sel_hi:[0,1]
	v_pk_mul_f32 v[24:25], v[178:179], v[0:1] op_sel_hi:[0,1]
	v_mfma_f32_16x16x32_bf16 v[0:3], v[142:145], v[20:23], 0
	v_mfma_f32_16x16x32_bf16 v[0:3], v[146:149], v[16:19], v[0:3]
	v_mul_f32_e64 v18, v176, v100
	v_mul_f32_e64 v19, v176, v101
	v_pk_mul_f32 v[16:17], v[176:177], v[98:99] op_sel_hi:[0,1]
	v_mfma_f32_16x16x32_bf16 v[0:3], v[150:153], v[8:11], v[0:3]
	v_mfma_f32_16x16x32_bf16 v[0:3], v[154:157], v[12:15], v[0:3]
	s_nop 7
	v_pk_mul_f32 v[10:11], v[28:29], v[2:3] op_sel_hi:[0,1]
	v_pk_mul_f32 v[8:9], v[28:29], v[0:1] op_sel_hi:[0,1]
	ds_read_b64_tr_b16 v[2:3], v214 offset:2560
	ds_read_b64_tr_b16 v[0:1], v214
	ds_read_b64_tr_b16 v[4:5], v214 offset:32
	ds_read_b64_tr_b16 v[12:13], v214 offset:5120
	ds_read_b64_tr_b16 v[14:15], v214 offset:7680
	s_waitcnt lgkmcnt(3)
	v_mfma_f32_16x16x32_bf16 v[94:97], v[0:3], v[30:33], v[94:97]
	v_mfma_f32_16x16x32_bf16 v[50:53], v[0:3], v[74:77], v[16:19]
	v_mfma_f32_16x16x32_bf16 v[16:19], v[0:3], v[78:81], v[102:105]
	v_mfma_f32_16x16x32_bf16 v[0:3], v[0:3], v[82:85], v[106:109]
	s_waitcnt lgkmcnt(0)
	v_mfma_f32_16x16x32_bf16 v[38:41], v[12:15], v[86:89], v[16:19]
	v_mfma_f32_16x16x32_bf16 v[12:15], v[12:15], v[90:93], v[0:3]
	ds_read_b64_tr_b16 v[6:7], v214 offset:2592
	s_nop 3
	ds_read_b64_tr_b16 v[0:1], v214 offset:5152
	ds_read_b64_tr_b16 v[2:3], v214 offset:7712
	s_waitcnt lgkmcnt(2)
	v_mfma_f32_16x16x32_bf16 v[62:65], v[4:7], v[30:33], v[110:113]
	v_mfma_f32_16x16x32_bf16 v[46:49], v[4:7], v[74:77], v[114:117]
	v_mfma_f32_16x16x32_bf16 v[16:19], v[4:7], v[78:81], v[118:121]
	v_mfma_f32_16x16x32_bf16 v[4:7], v[4:7], v[82:85], v[122:125]
	s_waitcnt lgkmcnt(0)
	v_mfma_f32_16x16x32_bf16 v[20:23], v[0:3], v[86:89], v[16:19]
	v_mfma_f32_16x16x32_bf16 v[4:7], v[0:3], v[90:93], v[4:7]
	ds_read_b64_tr_b16 v[0:1], v214 offset:64
	ds_read_b64_tr_b16 v[2:3], v214 offset:2624
	ds_read_b64_tr_b16 v[54:55], v214 offset:5184
	ds_read_b64_tr_b16 v[56:57], v214 offset:7744
	ds_read_b64_tr_b16 v[98:99], v214 offset:96
	ds_read_b64_tr_b16 v[100:101], v214 offset:2656
	ds_read_b64_tr_b16 v[102:103], v214 offset:5216
	ds_read_b64_tr_b16 v[104:105], v214 offset:7776
	s_waitcnt lgkmcnt(6)
	v_mfma_f32_16x16x32_bf16 v[58:61], v[0:3], v[30:33], v[126:129]
	v_mfma_f32_16x16x32_bf16 v[42:45], v[0:3], v[74:77], v[130:133]
	v_mfma_f32_16x16x32_bf16 v[16:19], v[0:3], v[78:81], v[134:137]
	v_mfma_f32_16x16x32_bf16 v[0:3], v[0:3], v[82:85], v[138:141]
	s_waitcnt lgkmcnt(4)
	v_mfma_f32_16x16x32_bf16 v[16:19], v[54:57], v[86:89], v[16:19]
	v_mfma_f32_16x16x32_bf16 v[0:3], v[54:57], v[90:93], v[0:3]
	s_waitcnt lgkmcnt(2)
	v_mfma_f32_16x16x32_bf16 v[54:57], v[98:101], v[30:33], v[66:69]
	v_add_u32_e32 v32, v209, v160
	v_mfma_f32_16x16x32_bf16 v[28:31], v[98:101], v[74:77], v[70:73]
	s_nop 0
	ds_read_b64 v[68:69], v32
	s_nop 0
	global_load_dword v70, v33, s[0:1]
	s_add_u32 s0, s2, s16
	s_addc_u32 s1, s3, s17
	v_mfma_f32_16x16x32_bf16 v[24:27], v[98:101], v[78:81], v[24:27]
	v_mov_b64_e32 v[78:79], s[0:1]
	v_mad_i64_i32 v[66:67], s[0:1], v174, s96, v[78:79]
	v_lshl_add_u64 v[72:73], v[66:67], 0, v[172:173]
	global_load_dwordx2 v[74:75], v[72:73], off
	global_load_dwordx2 v[202:203], v[72:73], off offset:32
	global_load_dwordx2 v[216:217], v[72:73], off offset:64
	global_load_dwordx2 v[248:249], v[72:73], off offset:96
	s_waitcnt lgkmcnt(0)
	v_lshlrev_b32_e32 v66, 16, v68
	v_and_b32_e32 v67, 0xffff0000, v68
	v_lshlrev_b32_e32 v68, 16, v69
	v_and_b32_e32 v69, 0xffff0000, v69
	v_mfma_f32_16x16x32_bf16 v[8:11], v[98:101], v[82:85], v[8:11]
	s_waitcnt vmcnt(4)
	v_pk_fma_f32 v[66:67], v[70:71], v[66:67], v[94:95] op_sel_hi:[0,1,1]
	v_pk_fma_f32 v[68:69], v[70:71], v[68:69], v[96:97] op_sel_hi:[0,1,1]
	v_mfma_f32_16x16x32_bf16 v[24:27], v[102:105], v[86:89], v[24:27]
	s_waitcnt vmcnt(3)
	v_lshlrev_b32_e32 v76, 16, v74
	v_mul_f32_e32 v32, 0xbfb8aa3b, v76
	v_exp_f32_e32 v32, v32
	v_and_b32_e32 v77, 0xffff0000, v74
	v_pk_mul_f32 v[66:67], v[66:67], v[76:77]
	v_lshlrev_b32_e32 v74, 16, v75
	v_add_f32_e32 v32, 1.0, v32
	v_rcp_f32_e32 v80, v32
	v_mul_f32_e32 v32, 0xbfb8aa3b, v77
	v_exp_f32_e32 v32, v32
	v_and_b32_e32 v75, 0xffff0000, v75
	v_pk_mul_f32 v[68:69], v[68:69], v[74:75]
	v_mfma_f32_16x16x32_bf16 v[8:11], v[102:105], v[90:93], v[8:11]
	v_add_f32_e32 v32, 1.0, v32
	v_rcp_f32_e32 v81, v32
	s_nop 0
	v_pk_mul_f32 v[66:67], v[66:67], v[80:81]
	s_nop 0
	v_mul_f32_e32 v32, v67, v67
	v_pk_fma_f32 v[76:77], v[66:67], v[66:67], v[32:33] op_sel_hi:[1,1,0]
	v_mul_f32_e32 v32, 0xbfb8aa3b, v74
	v_exp_f32_e32 v32, v32
	s_nop 0
	v_add_f32_e32 v32, 1.0, v32
	v_rcp_f32_e32 v80, v32
	v_mul_f32_e32 v32, 0xbfb8aa3b, v75
	v_exp_f32_e32 v32, v32
	s_nop 0
	v_add_f32_e32 v32, 1.0, v32
	v_rcp_f32_e32 v81, v32
	s_nop 0
	v_pk_mul_f32 v[68:69], v[68:69], v[80:81]
	v_pk_fma_f32 v[74:75], v[68:69], v[68:69], v[76:77]
	v_mul_f32_e32 v32, v69, v69
	v_pk_add_f32 v[74:75], v[32:33], v[74:75] op_sel_hi:[0,1]
	v_add_u32_e32 v32, v209, v189
	ds_read_b64 v[76:77], v32
	s_waitcnt lgkmcnt(0)
	v_lshlrev_b32_e32 v82, 16, v76
	v_and_b32_e32 v83, 0xffff0000, v76
	v_pk_fma_f32 v[62:63], v[70:71], v[82:83], v[62:63] op_sel_hi:[0,1,1]
	v_lshlrev_b32_e32 v76, 16, v77
	v_and_b32_e32 v77, 0xffff0000, v77
	v_pk_fma_f32 v[64:65], v[70:71], v[76:77], v[64:65] op_sel_hi:[0,1,1]
	s_waitcnt vmcnt(2)
	v_mov_b64_e32 v[80:81], v[202:203]
	v_lshlrev_b32_e32 v84, 16, v80
	v_mul_f32_e32 v32, 0xbfb8aa3b, v84
	v_exp_f32_e32 v32, v32
	v_and_b32_e32 v85, 0xffff0000, v80
	v_pk_mul_f32 v[62:63], v[62:63], v[84:85]
	v_lshlrev_b32_e32 v80, 16, v81
	v_add_f32_e32 v32, 1.0, v32
	v_rcp_f32_e32 v86, v32
	v_mul_f32_e32 v32, 0xbfb8aa3b, v85
	v_exp_f32_e32 v32, v32
	v_and_b32_e32 v81, 0xffff0000, v81
	v_pk_mul_f32 v[64:65], v[64:65], v[80:81]
	v_add_f32_e32 v32, 1.0, v32
	v_rcp_f32_e32 v87, v32
	s_nop 0
	v_pk_mul_f32 v[62:63], v[62:63], v[86:87]
	s_nop 0
	v_pk_fma_f32 v[74:75], v[62:63], v[62:63], v[74:75]
	v_mul_f32_e32 v32, v63, v63
	v_pk_add_f32 v[74:75], v[32:33], v[74:75] op_sel_hi:[0,1]
	v_mul_f32_e32 v32, 0xbfb8aa3b, v80
	v_exp_f32_e32 v32, v32
	s_nop 0
	v_add_f32_e32 v32, 1.0, v32
	v_rcp_f32_e32 v82, v32
	v_mul_f32_e32 v32, 0xbfb8aa3b, v81
	v_exp_f32_e32 v32, v32
	s_waitcnt vmcnt(1)
	v_mov_b64_e32 v[80:81], v[216:217]
	v_lshlrev_b32_e32 v84, 16, v80
	v_add_f32_e32 v32, 1.0, v32
	v_rcp_f32_e32 v83, v32
	v_and_b32_e32 v85, 0xffff0000, v80
	v_lshlrev_b32_e32 v80, 16, v81
	v_and_b32_e32 v81, 0xffff0000, v81
	v_pk_mul_f32 v[64:65], v[64:65], v[82:83]
	s_nop 0
	v_pk_fma_f32 v[74:75], v[64:65], v[64:65], v[74:75]
	v_mul_f32_e32 v32, v65, v65
	v_pk_add_f32 v[74:75], v[32:33], v[74:75] op_sel_hi:[0,1]
	v_add_u32_e32 v32, v209, v188
	ds_read_b64 v[76:77], v32
	v_mul_f32_e32 v32, 0xbfb8aa3b, v84
	v_exp_f32_e32 v32, v32
	s_waitcnt lgkmcnt(0)
	v_lshlrev_b32_e32 v82, 16, v76
	v_add_f32_e32 v32, 1.0, v32
	v_rcp_f32_e32 v86, v32
	v_mul_f32_e32 v32, 0xbfb8aa3b, v85
	v_exp_f32_e32 v32, v32
	v_and_b32_e32 v83, 0xffff0000, v76
	v_pk_fma_f32 v[58:59], v[70:71], v[82:83], v[58:59] op_sel_hi:[0,1,1]
	v_pk_mul_f32 v[58:59], v[58:59], v[84:85]
	v_add_f32_e32 v32, 1.0, v32
	v_rcp_f32_e32 v87, v32
	v_lshlrev_b32_e32 v76, 16, v77
	v_and_b32_e32 v77, 0xffff0000, v77
	v_pk_fma_f32 v[60:61], v[70:71], v[76:77], v[60:61] op_sel_hi:[0,1,1]
	v_pk_mul_f32 v[58:59], v[58:59], v[86:87]
	v_pk_mul_f32 v[60:61], v[60:61], v[80:81]
	v_pk_fma_f32 v[74:75], v[58:59], v[58:59], v[74:75]
	v_mul_f32_e32 v32, v59, v59
	v_pk_add_f32 v[74:75], v[32:33], v[74:75] op_sel_hi:[0,1]
	v_mul_f32_e32 v32, 0xbfb8aa3b, v80
	v_exp_f32_e32 v32, v32
	s_nop 0
	v_add_f32_e32 v32, 1.0, v32
	v_rcp_f32_e32 v82, v32
	v_mul_f32_e32 v32, 0xbfb8aa3b, v81
	v_exp_f32_e32 v32, v32
	s_nop 0
	v_add_f32_e32 v32, 1.0, v32
	v_rcp_f32_e32 v83, v32
	s_nop 0
	v_pk_mul_f32 v[60:61], v[60:61], v[82:83]
	s_nop 0
	v_pk_fma_f32 v[74:75], v[60:61], v[60:61], v[74:75]
	v_mul_f32_e32 v32, v61, v61
	v_pk_add_f32 v[74:75], v[32:33], v[74:75] op_sel_hi:[0,1]
	v_add_u32_e32 v32, v209, v187
	ds_read_b64 v[76:77], v32
	s_waitcnt lgkmcnt(0)
	v_lshlrev_b32_e32 v72, 16, v76
	v_and_b32_e32 v73, 0xffff0000, v76
	v_pk_fma_f32 v[54:55], v[70:71], v[72:73], v[54:55] op_sel_hi:[0,1,1]
	s_waitcnt vmcnt(0)
	v_mov_b64_e32 v[80:81], v[248:249]
	v_lshlrev_b32_e32 v82, 16, v80
	v_mul_f32_e32 v32, 0xbfb8aa3b, v82
	v_exp_f32_e32 v32, v32
	v_and_b32_e32 v83, 0xffff0000, v80
	v_pk_mul_f32 v[54:55], v[54:55], v[82:83]
	v_lshlrev_b32_e32 v76, 16, v81
	v_add_f32_e32 v32, 1.0, v32
	v_rcp_f32_e32 v84, v32
	v_mul_f32_e32 v32, 0xbfb8aa3b, v83
	v_exp_f32_e32 v32, v32
	s_nop 0
	v_add_f32_e32 v32, 1.0, v32
	v_rcp_f32_e32 v85, v32
	s_nop 0
	v_pk_mul_f32 v[72:73], v[54:55], v[84:85]
	s_nop 0
	v_pk_fma_f32 v[54:55], v[72:73], v[72:73], v[74:75]
	v_mul_f32_e32 v32, v73, v73
	v_pk_add_f32 v[54:55], v[32:33], v[54:55] op_sel_hi:[0,1]
	v_mul_f32_e32 v32, 0xbfb8aa3b, v76
	v_exp_f32_e32 v32, v32
	v_lshlrev_b32_e32 v74, 16, v77
	v_and_b32_e32 v75, 0xffff0000, v77
	v_and_b32_e32 v77, 0xffff0000, v81
	v_add_f32_e32 v32, 1.0, v32
	v_rcp_f32_e32 v80, v32
	v_mul_f32_e32 v32, 0xbfb8aa3b, v77
	v_exp_f32_e32 v32, v32
	v_pk_fma_f32 v[56:57], v[70:71], v[74:75], v[56:57] op_sel_hi:[0,1,1]
	v_pk_mul_f32 v[56:57], v[56:57], v[76:77]
	v_or_b32_e32 v76, s55, v185
	v_add_f32_e32 v32, 1.0, v32
	v_rcp_f32_e32 v81, v32
	s_nop 0
	v_pk_mul_f32 v[56:57], v[56:57], v[80:81]
	s_nop 0
	v_pk_fma_f32 v[54:55], v[56:57], v[56:57], v[54:55]
	v_mul_f32_e32 v32, v57, v57
	v_pk_add_f32 v[110:111], v[32:33], v[54:55] op_sel_hi:[0,1]
	v_or_b32_e32 v54, s55, v184
	v_mad_i64_i32 v[74:75], s[0:1], v54, s96, v[78:79]
	v_lshl_add_u64 v[74:75], v[74:75], 0, v[172:173]
	global_load_dwordx2 v[126:127], v[74:75], off
	global_load_dwordx2 v[122:123], v[74:75], off offset:32
	global_load_dwordx2 v[116:117], v[74:75], off offset:64
	global_load_dwordx2 v[112:113], v[74:75], off offset:96
	v_mad_i64_i32 v[74:75], s[0:1], v76, s96, v[78:79]
	v_lshl_add_u64 v[74:75], v[74:75], 0, v[172:173]
	global_load_dwordx2 v[106:107], v[74:75], off
	global_load_dwordx2 v[102:103], v[74:75], off offset:32
	global_load_dwordx2 v[98:99], v[74:75], off offset:64
	global_load_dwordx2 v[94:95], v[74:75], off offset:96
	v_or_b32_e32 v74, s55, v186
	v_mad_i64_i32 v[78:79], s[0:1], v74, s96, v[78:79]
	v_lshl_add_u64 v[78:79], v[78:79], 0, v[172:173]
	global_load_dwordx2 v[90:91], v[78:79], off
	global_load_dwordx2 v[86:87], v[78:79], off offset:32
	global_load_dwordx2 v[82:83], v[78:79], off offset:64
	v_add_u32_e32 v32, v211, v160
	global_load_dwordx2 v[78:79], v[78:79], off offset:96
	ds_read_b64 v[120:121], v32
	v_add_u32_e32 v32, v211, v189
	ds_read_b64 v[124:125], v32
	v_add_u32_e32 v32, v211, v188
	ds_read_b64 v[118:119], v32
	v_add_u32_e32 v32, v211, v187
	ds_read_b64 v[114:115], v32
	v_add_u32_e32 v32, v212, v160
	ds_read_b64 v[108:109], v32
	v_add_u32_e32 v32, v212, v189
	ds_read_b64 v[104:105], v32
	v_add_u32_e32 v32, v212, v188
	ds_read_b64 v[100:101], v32
	v_add_u32_e32 v32, v212, v187
	ds_read_b64 v[96:97], v32
	v_add_u32_e32 v32, v210, v160
	ds_read_b64 v[92:93], v32
	v_add_u32_e32 v32, v210, v189
	ds_read_b64 v[88:89], v32
	v_add_u32_e32 v32, v210, v188
	ds_read_b64 v[84:85], v32
	v_add_u32_e32 v32, v210, v187
	ds_read_b64 v[80:81], v32
	s_lshl_b32 s0, s33, 11
	v_mov_b32_e32 v55, v110
	s_add_i32 s16, s0, 0
	s_nop 0
	v_permlane16_swap_b32_e32 v110, v55
	s_add_i32 s16, s16, 0x15000
	v_add_f32_e32 v55, v110, v55
	s_add_i32 s0, s16, s35
	v_mov_b32_e32 v71, v55
	v_lshl_add_u32 v32, v166, 2, s0
	s_nop 0
	v_permlane32_swap_b32_e32 v55, v71
	s_and_saveexec_b64 s[0:1], s[42:43]
	v_add_f32_e32 v55, v55, v71
	ds_write_b32 v32, v55
	s_or_b64 exec, exec, s[0:1]
	s_waitcnt vmcnt(11)
	v_lshlrev_b32_e32 v128, 16, v126
	v_mul_f32_e32 v55, 0xbfb8aa3b, v128
	v_exp_f32_e32 v55, v55
	v_and_b32_e32 v129, 0xffff0000, v126
	v_lshlrev_b32_e32 v126, 16, v127
	v_mov_b32_e32 v71, v70
	v_add_f32_e32 v55, 1.0, v55
	v_rcp_f32_e32 v130, v55
	v_mul_f32_e32 v55, 0xbfb8aa3b, v129
	v_exp_f32_e32 v55, v55
	s_waitcnt lgkmcnt(11)
	v_lshlrev_b32_e32 v110, 16, v120
	v_and_b32_e32 v111, 0xffff0000, v120
	v_pk_fma_f32 v[50:51], v[70:71], v[110:111], v[50:51]
	v_add_f32_e32 v55, 1.0, v55
	v_rcp_f32_e32 v131, v55
	v_mul_f32_e32 v55, 0xbfb8aa3b, v126
	v_exp_f32_e32 v55, v55
	v_and_b32_e32 v127, 0xffff0000, v127
	v_pk_mul_f32 v[50:51], v[50:51], v[128:129]
	v_lshlrev_b32_e32 v120, 16, v121
	v_add_f32_e32 v55, 1.0, v55
	v_rcp_f32_e32 v128, v55
	v_mul_f32_e32 v55, 0xbfb8aa3b, v127
	v_exp_f32_e32 v55, v55
	v_and_b32_e32 v121, 0xffff0000, v121
	v_pk_fma_f32 v[52:53], v[70:71], v[120:121], v[52:53]
	v_pk_mul_f32 v[50:51], v[50:51], v[130:131]
	v_pk_mul_f32 v[52:53], v[52:53], v[126:127]
	v_add_f32_e32 v55, 1.0, v55
	s_waitcnt vmcnt(10)
	v_lshlrev_b32_e32 v126, 16, v122
	v_rcp_f32_e32 v129, v55
	v_mul_f32_e32 v55, 0xbfb8aa3b, v126
	v_exp_f32_e32 v55, v55
	v_and_b32_e32 v127, 0xffff0000, v122
	v_pk_mul_f32 v[52:53], v[52:53], v[128:129]
	v_lshlrev_b32_e32 v122, 16, v123
	v_add_f32_e32 v55, 1.0, v55
	v_rcp_f32_e32 v128, v55
	v_mul_f32_e32 v55, 0xbfb8aa3b, v127
	v_exp_f32_e32 v55, v55
	v_mul_f32_e32 v110, v51, v51
	v_pk_fma_f32 v[110:111], v[50:51], v[50:51], v[110:111] op_sel_hi:[1,1,0]
	v_mul_f32_e32 v120, v53, v53
	v_add_f32_e32 v55, 1.0, v55
	v_rcp_f32_e32 v129, v55
	v_mul_f32_e32 v55, 0xbfb8aa3b, v122
	v_exp_f32_e32 v55, v55
	v_pk_fma_f32 v[110:111], v[52:53], v[52:53], v[110:111]
	v_and_b32_e32 v123, 0xffff0000, v123
	v_pk_add_f32 v[110:111], v[120:121], v[110:111] op_sel_hi:[0,1]
	s_waitcnt lgkmcnt(10)
	v_lshlrev_b32_e32 v120, 16, v124
	v_and_b32_e32 v121, 0xffff0000, v124
	v_pk_fma_f32 v[46:47], v[70:71], v[120:121], v[46:47]
	v_add_f32_e32 v55, 1.0, v55
	v_pk_mul_f32 v[46:47], v[46:47], v[126:127]
	v_rcp_f32_e32 v124, v55
	v_mul_f32_e32 v55, 0xbfb8aa3b, v123
	v_pk_mul_f32 v[46:47], v[46:47], v[128:129]
	v_exp_f32_e32 v55, v55
	v_pk_fma_f32 v[110:111], v[46:47], v[46:47], v[110:111]
	v_mul_f32_e32 v120, v47, v47
	v_pk_add_f32 v[110:111], v[120:121], v[110:111] op_sel_hi:[0,1]
	v_lshlrev_b32_e32 v120, 16, v125
	v_and_b32_e32 v121, 0xffff0000, v125
	v_pk_fma_f32 v[48:49], v[70:71], v[120:121], v[48:49]
	v_add_f32_e32 v55, 1.0, v55
	v_pk_mul_f32 v[48:49], v[48:49], v[122:123]
	s_waitcnt vmcnt(9)
	v_lshlrev_b32_e32 v122, 16, v116
	v_rcp_f32_e32 v125, v55
	v_mul_f32_e32 v55, 0xbfb8aa3b, v122
	v_exp_f32_e32 v55, v55
	v_and_b32_e32 v123, 0xffff0000, v116
	v_pk_mul_f32 v[48:49], v[48:49], v[124:125]
	v_add_f32_e32 v55, 1.0, v55
	v_rcp_f32_e32 v124, v55
	v_mul_f32_e32 v55, 0xbfb8aa3b, v123
	v_exp_f32_e32 v55, v55
	v_pk_fma_f32 v[110:111], v[48:49], v[48:49], v[110:111]
	v_mul_f32_e32 v120, v49, v49
	v_pk_add_f32 v[110:111], v[120:121], v[110:111] op_sel_hi:[0,1]
	v_add_f32_e32 v55, 1.0, v55
	v_rcp_f32_e32 v125, v55
	s_waitcnt lgkmcnt(9)
	v_lshlrev_b32_e32 v120, 16, v118
	v_and_b32_e32 v121, 0xffff0000, v118
	v_pk_fma_f32 v[42:43], v[70:71], v[120:121], v[42:43]
	v_lshlrev_b32_e32 v118, 16, v119
	v_pk_mul_f32 v[42:43], v[42:43], v[122:123]
	v_and_b32_e32 v119, 0xffff0000, v119
	v_pk_mul_f32 v[42:43], v[42:43], v[124:125]
	v_pk_fma_f32 v[44:45], v[70:71], v[118:119], v[44:45]
	v_pk_fma_f32 v[110:111], v[42:43], v[42:43], v[110:111]
	v_mul_f32_e32 v116, v43, v43
	v_pk_add_f32 v[110:111], v[116:117], v[110:111] op_sel_hi:[0,1]
	v_lshlrev_b32_e32 v116, 16, v117
	v_mul_f32_e32 v55, 0xbfb8aa3b, v116
	v_exp_f32_e32 v55, v55
	v_and_b32_e32 v117, 0xffff0000, v117
	s_waitcnt vmcnt(8)
	v_lshlrev_b32_e32 v118, 16, v112
	v_pk_mul_f32 v[44:45], v[44:45], v[116:117]
	v_add_f32_e32 v55, 1.0, v55
	v_rcp_f32_e32 v120, v55
	v_mul_f32_e32 v55, 0xbfb8aa3b, v117
	v_exp_f32_e32 v55, v55
	v_and_b32_e32 v119, 0xffff0000, v112
	v_add_f32_e32 v55, 1.0, v55
	v_rcp_f32_e32 v121, v55
	v_mul_f32_e32 v55, 0xbfb8aa3b, v118
	v_exp_f32_e32 v55, v55
	v_pk_mul_f32 v[44:45], v[44:45], v[120:121]
	s_nop 0
	v_pk_fma_f32 v[110:111], v[44:45], v[44:45], v[110:111]
	v_add_f32_e32 v55, 1.0, v55
	v_rcp_f32_e32 v120, v55
	v_mul_f32_e32 v55, 0xbfb8aa3b, v119
	v_exp_f32_e32 v55, v55
	v_mul_f32_e32 v116, v45, v45
	v_pk_add_f32 v[110:111], v[116:117], v[110:111] op_sel_hi:[0,1]
	s_waitcnt lgkmcnt(8)
	v_lshlrev_b32_e32 v116, 16, v114
	v_add_f32_e32 v55, 1.0, v55
	v_rcp_f32_e32 v121, v55
	v_and_b32_e32 v117, 0xffff0000, v114
	v_pk_fma_f32 v[28:29], v[70:71], v[116:117], v[28:29]
	v_lshlrev_b32_e32 v114, 16, v115
	v_pk_mul_f32 v[28:29], v[28:29], v[118:119]
	v_and_b32_e32 v115, 0xffff0000, v115
	v_pk_mul_f32 v[28:29], v[28:29], v[120:121]
	v_pk_fma_f32 v[30:31], v[70:71], v[114:115], v[30:31]
	v_pk_fma_f32 v[110:111], v[28:29], v[28:29], v[110:111]
	v_mul_f32_e32 v112, v29, v29
	v_pk_add_f32 v[110:111], v[112:113], v[110:111] op_sel_hi:[0,1]
	v_lshlrev_b32_e32 v112, 16, v113
	v_mul_f32_e32 v55, 0xbfb8aa3b, v112
	v_exp_f32_e32 v55, v55
	v_and_b32_e32 v113, 0xffff0000, v113
	v_pk_mul_f32 v[30:31], v[30:31], v[112:113]
	v_add_f32_e32 v55, 1.0, v55
	v_rcp_f32_e32 v116, v55
	v_mul_f32_e32 v55, 0xbfb8aa3b, v113
	v_exp_f32_e32 v55, v55
	s_nop 0
	v_add_f32_e32 v55, 1.0, v55
	v_rcp_f32_e32 v117, v55
	s_nop 0
	v_pk_mul_f32 v[30:31], v[30:31], v[116:117]
	s_nop 0
	v_pk_fma_f32 v[110:111], v[30:31], v[30:31], v[110:111]
	v_mul_f32_e32 v112, v31, v31
	v_pk_add_f32 v[110:111], v[112:113], v[110:111] op_sel_hi:[0,1]
	v_mov_b32_e32 v55, v110
	s_nop 1
	v_permlane16_swap_b32_e32 v110, v55
	v_add_f32_e32 v55, v110, v55
	v_mov_b32_e32 v75, v55
	s_nop 1
	v_permlane32_swap_b32_e32 v55, v75
	s_and_saveexec_b64 s[0:1], s[42:43]
	v_add_f32_e32 v55, v55, v75
	ds_write_b32 v32, v55 offset:64
	s_or_b64 exec, exec, s[0:1]
	s_waitcnt vmcnt(7)
	v_lshlrev_b32_e32 v112, 16, v106
	v_mul_f32_e32 v55, 0xbfb8aa3b, v112
	v_exp_f32_e32 v55, v55
	v_and_b32_e32 v113, 0xffff0000, v106
	s_waitcnt lgkmcnt(7)
	v_lshlrev_b32_e32 v110, 16, v108
	v_and_b32_e32 v111, 0xffff0000, v108
	v_add_f32_e32 v55, 1.0, v55
	v_rcp_f32_e32 v114, v55
	v_mul_f32_e32 v55, 0xbfb8aa3b, v113
	v_exp_f32_e32 v55, v55
	v_pk_fma_f32 v[38:39], v[70:71], v[110:111], v[38:39]
	v_lshlrev_b32_e32 v108, 16, v109
	v_pk_mul_f32 v[38:39], v[38:39], v[112:113]
	v_add_f32_e32 v55, 1.0, v55
	v_rcp_f32_e32 v115, v55
	v_and_b32_e32 v109, 0xffff0000, v109
	v_pk_fma_f32 v[40:41], v[70:71], v[108:109], v[40:41]
	v_pk_mul_f32 v[38:39], v[38:39], v[114:115]
	s_nop 0
	v_mul_f32_e32 v106, v39, v39
	v_pk_fma_f32 v[110:111], v[38:39], v[38:39], v[106:107] op_sel_hi:[1,1,0]
	v_lshlrev_b32_e32 v106, 16, v107
	v_mul_f32_e32 v55, 0xbfb8aa3b, v106
	v_exp_f32_e32 v55, v55
	v_and_b32_e32 v107, 0xffff0000, v107
	v_pk_mul_f32 v[40:41], v[40:41], v[106:107]
	v_add_f32_e32 v55, 1.0, v55
	v_rcp_f32_e32 v112, v55
	v_mul_f32_e32 v55, 0xbfb8aa3b, v107
	v_exp_f32_e32 v55, v55
	s_nop 0
	v_add_f32_e32 v55, 1.0, v55
	v_rcp_f32_e32 v113, v55
	s_nop 0
	v_pk_mul_f32 v[40:41], v[40:41], v[112:113]
	s_nop 0
	v_pk_fma_f32 v[106:107], v[40:41], v[40:41], v[110:111]
	s_waitcnt vmcnt(6)
	v_lshlrev_b32_e32 v110, 16, v102
	v_mul_f32_e32 v55, 0xbfb8aa3b, v110
	v_exp_f32_e32 v55, v55
	v_and_b32_e32 v111, 0xffff0000, v102
	v_mul_f32_e32 v108, v41, v41
	v_pk_add_f32 v[106:107], v[108:109], v[106:107] op_sel_hi:[0,1]
	v_add_f32_e32 v55, 1.0, v55
	v_rcp_f32_e32 v112, v55
	v_mul_f32_e32 v55, 0xbfb8aa3b, v111
	v_exp_f32_e32 v55, v55
	s_waitcnt lgkmcnt(6)
	v_lshlrev_b32_e32 v108, 16, v104
	v_and_b32_e32 v109, 0xffff0000, v104
	v_pk_fma_f32 v[20:21], v[70:71], v[108:109], v[20:21]
	v_add_f32_e32 v55, 1.0, v55
	v_rcp_f32_e32 v113, v55
	v_pk_mul_f32 v[20:21], v[20:21], v[110:111]
	v_lshlrev_b32_e32 v104, 16, v105
	v_and_b32_e32 v105, 0xffff0000, v105
	v_pk_mul_f32 v[20:21], v[20:21], v[112:113]
	v_pk_fma_f32 v[22:23], v[70:71], v[104:105], v[22:23]
	v_pk_fma_f32 v[106:107], v[20:21], v[20:21], v[106:107]
	v_mul_f32_e32 v102, v21, v21
	v_pk_add_f32 v[106:107], v[102:103], v[106:107] op_sel_hi:[0,1]
	v_lshlrev_b32_e32 v102, 16, v103
	v_mul_f32_e32 v55, 0xbfb8aa3b, v102
	v_exp_f32_e32 v55, v55
	v_and_b32_e32 v103, 0xffff0000, v103
	v_pk_mul_f32 v[22:23], v[22:23], v[102:103]
	v_add_f32_e32 v55, 1.0, v55
	v_rcp_f32_e32 v108, v55
	v_mul_f32_e32 v55, 0xbfb8aa3b, v103
	v_exp_f32_e32 v55, v55
	s_nop 0
	v_add_f32_e32 v55, 1.0, v55
	v_rcp_f32_e32 v109, v55
	s_nop 0
	v_pk_mul_f32 v[22:23], v[22:23], v[108:109]
	s_nop 0
	v_pk_fma_f32 v[102:103], v[22:23], v[22:23], v[106:107]
	s_waitcnt vmcnt(5)
	v_lshlrev_b32_e32 v106, 16, v98
	v_mul_f32_e32 v55, 0xbfb8aa3b, v106
	v_exp_f32_e32 v55, v55
	v_and_b32_e32 v107, 0xffff0000, v98
	v_mul_f32_e32 v104, v23, v23
	v_pk_add_f32 v[102:103], v[104:105], v[102:103] op_sel_hi:[0,1]
	v_add_f32_e32 v55, 1.0, v55
	v_rcp_f32_e32 v108, v55
	v_mul_f32_e32 v55, 0xbfb8aa3b, v107
	v_exp_f32_e32 v55, v55
	s_waitcnt lgkmcnt(5)
	v_lshlrev_b32_e32 v104, 16, v100
	v_and_b32_e32 v105, 0xffff0000, v100
	v_pk_fma_f32 v[16:17], v[70:71], v[104:105], v[16:17]
	v_add_f32_e32 v55, 1.0, v55
	v_rcp_f32_e32 v109, v55
	v_pk_mul_f32 v[16:17], v[16:17], v[106:107]
	v_lshlrev_b32_e32 v100, 16, v101
	v_and_b32_e32 v101, 0xffff0000, v101
	v_pk_mul_f32 v[16:17], v[16:17], v[108:109]
	v_pk_fma_f32 v[18:19], v[70:71], v[100:101], v[18:19]
	v_pk_fma_f32 v[102:103], v[16:17], v[16:17], v[102:103]
	v_mul_f32_e32 v98, v17, v17
	v_pk_add_f32 v[102:103], v[98:99], v[102:103] op_sel_hi:[0,1]
	v_lshlrev_b32_e32 v98, 16, v99
	v_mul_f32_e32 v55, 0xbfb8aa3b, v98
	v_exp_f32_e32 v55, v55
	v_and_b32_e32 v99, 0xffff0000, v99
	v_pk_mul_f32 v[18:19], v[18:19], v[98:99]
	v_add_f32_e32 v55, 1.0, v55
	v_rcp_f32_e32 v104, v55
	v_mul_f32_e32 v55, 0xbfb8aa3b, v99
	v_exp_f32_e32 v55, v55
	s_nop 0
	v_add_f32_e32 v55, 1.0, v55
	v_rcp_f32_e32 v105, v55
	s_nop 0
	v_pk_mul_f32 v[18:19], v[18:19], v[104:105]
	s_nop 0
	v_pk_fma_f32 v[98:99], v[18:19], v[18:19], v[102:103]
	s_waitcnt vmcnt(4)
	v_lshlrev_b32_e32 v102, 16, v94
	v_mul_f32_e32 v55, 0xbfb8aa3b, v102
	v_exp_f32_e32 v55, v55
	v_and_b32_e32 v103, 0xffff0000, v94
	v_mul_f32_e32 v100, v19, v19
	v_pk_add_f32 v[98:99], v[100:101], v[98:99] op_sel_hi:[0,1]
	v_add_f32_e32 v55, 1.0, v55
	v_rcp_f32_e32 v104, v55
	v_mul_f32_e32 v55, 0xbfb8aa3b, v103
	v_exp_f32_e32 v55, v55
	s_waitcnt lgkmcnt(4)
	v_lshlrev_b32_e32 v100, 16, v96
	v_and_b32_e32 v101, 0xffff0000, v96
	v_pk_fma_f32 v[24:25], v[70:71], v[100:101], v[24:25]
	v_add_f32_e32 v55, 1.0, v55
	v_rcp_f32_e32 v105, v55
	v_pk_mul_f32 v[24:25], v[24:25], v[102:103]
	v_lshlrev_b32_e32 v96, 16, v97
	v_and_b32_e32 v97, 0xffff0000, v97
	v_pk_mul_f32 v[24:25], v[24:25], v[104:105]
	v_pk_fma_f32 v[26:27], v[70:71], v[96:97], v[26:27]
	v_pk_fma_f32 v[98:99], v[24:25], v[24:25], v[98:99]
	v_mul_f32_e32 v94, v25, v25
	v_pk_add_f32 v[98:99], v[94:95], v[98:99] op_sel_hi:[0,1]
	v_lshlrev_b32_e32 v94, 16, v95
	v_mul_f32_e32 v55, 0xbfb8aa3b, v94
	v_exp_f32_e32 v55, v55
	v_and_b32_e32 v95, 0xffff0000, v95
	v_pk_mul_f32 v[26:27], v[26:27], v[94:95]
	v_add_f32_e32 v55, 1.0, v55
	v_rcp_f32_e32 v100, v55
	v_mul_f32_e32 v55, 0xbfb8aa3b, v95
	v_exp_f32_e32 v55, v55
	s_nop 0
	v_add_f32_e32 v55, 1.0, v55
	v_rcp_f32_e32 v101, v55
	s_nop 0
	v_pk_mul_f32 v[26:27], v[26:27], v[100:101]
	s_nop 0
	v_pk_fma_f32 v[94:95], v[26:27], v[26:27], v[98:99]
	v_mul_f32_e32 v96, v27, v27
	v_pk_add_f32 v[94:95], v[96:97], v[94:95] op_sel_hi:[0,1]
	v_mov_b32_e32 v55, v94
	s_nop 1
	v_permlane16_swap_b32_e32 v94, v55
	v_add_f32_e32 v55, v94, v55
	v_mov_b32_e32 v75, v55
	s_nop 1
	v_permlane32_swap_b32_e32 v55, v75
	s_and_saveexec_b64 s[0:1], s[42:43]
	v_add_f32_e32 v55, v55, v75
	ds_write_b32 v32, v55 offset:128
	s_or_b64 exec, exec, s[0:1]
	s_waitcnt vmcnt(3)
	v_lshlrev_b32_e32 v96, 16, v90
	v_mul_f32_e32 v55, 0xbfb8aa3b, v96
	v_exp_f32_e32 v55, v55
	v_and_b32_e32 v97, 0xffff0000, v90
	v_lshlrev_b32_e32 v90, 16, v91
	s_waitcnt lgkmcnt(3)
	v_lshlrev_b32_e32 v94, 16, v92
	v_add_f32_e32 v55, 1.0, v55
	v_rcp_f32_e32 v98, v55
	v_mul_f32_e32 v55, 0xbfb8aa3b, v97
	v_exp_f32_e32 v55, v55
	v_and_b32_e32 v95, 0xffff0000, v92
	v_pk_fma_f32 v[12:13], v[70:71], v[94:95], v[12:13]
	v_and_b32_e32 v91, 0xffff0000, v91
	v_add_f32_e32 v55, 1.0, v55
	v_rcp_f32_e32 v99, v55
	v_mul_f32_e32 v55, 0xbfb8aa3b, v90
	v_exp_f32_e32 v55, v55
	v_pk_mul_f32 v[12:13], v[12:13], v[96:97]
	v_lshlrev_b32_e32 v92, 16, v93
	v_and_b32_e32 v93, 0xffff0000, v93
	v_add_f32_e32 v55, 1.0, v55
	v_rcp_f32_e32 v96, v55
	v_mul_f32_e32 v55, 0xbfb8aa3b, v91
	v_exp_f32_e32 v55, v55
	v_pk_mul_f32 v[94:95], v[12:13], v[98:99]
	v_pk_fma_f32 v[14:15], v[70:71], v[92:93], v[14:15]
	v_mul_f32_e32 v12, v95, v95
	v_add_f32_e32 v55, 1.0, v55
	v_rcp_f32_e32 v97, v55
	v_pk_mul_f32 v[14:15], v[14:15], v[90:91]
	v_pk_fma_f32 v[12:13], v[94:95], v[94:95], v[12:13] op_sel_hi:[1,1,0]
	s_waitcnt vmcnt(2)
	v_lshlrev_b32_e32 v92, 16, v86
	v_pk_mul_f32 v[90:91], v[14:15], v[96:97]
	v_and_b32_e32 v93, 0xffff0000, v86
	v_pk_fma_f32 v[12:13], v[90:91], v[90:91], v[12:13]
	v_mul_f32_e32 v14, v91, v91
	v_pk_add_f32 v[12:13], v[14:15], v[12:13] op_sel_hi:[0,1]
	s_waitcnt lgkmcnt(2)
	v_lshlrev_b32_e32 v14, 16, v88
	v_and_b32_e32 v15, 0xffff0000, v88
	v_mul_f32_e32 v55, 0xbfb8aa3b, v92
	v_pk_fma_f32 v[4:5], v[70:71], v[14:15], v[4:5]
	v_mul_f32_e32 v14, 0xbfb8aa3b, v93
	v_exp_f32_e32 v55, v55
	v_exp_f32_e32 v14, v14
	v_pk_mul_f32 v[4:5], v[4:5], v[92:93]
	v_and_b32_e32 v15, 0xffff0000, v87
	v_add_f32_e32 v55, 1.0, v55
	v_add_f32_e32 v14, 1.0, v14
	v_rcp_f32_e32 v96, v55
	v_rcp_f32_e32 v97, v14
	v_lshlrev_b32_e32 v14, 16, v87
	v_mul_f32_e32 v55, 0xbfb8aa3b, v14
	v_exp_f32_e32 v55, v55
	v_pk_mul_f32 v[92:93], v[4:5], v[96:97]
	v_add_f32_e32 v55, 1.0, v55
	v_pk_fma_f32 v[4:5], v[92:93], v[92:93], v[12:13]
	v_mul_f32_e32 v12, v93, v93
	v_pk_add_f32 v[4:5], v[12:13], v[4:5] op_sel_hi:[0,1]
	v_lshlrev_b32_e32 v12, 16, v89
	v_and_b32_e32 v13, 0xffff0000, v89
	v_pk_fma_f32 v[6:7], v[70:71], v[12:13], v[6:7]
	v_mul_f32_e32 v12, 0xbfb8aa3b, v15
	v_exp_f32_e32 v12, v12
	v_rcp_f32_e32 v86, v55
	v_pk_mul_f32 v[6:7], v[6:7], v[14:15]
	s_waitcnt vmcnt(1)
	v_and_b32_e32 v13, 0xffff0000, v82
	v_add_f32_e32 v12, 1.0, v12
	v_rcp_f32_e32 v87, v12
	v_lshlrev_b32_e32 v12, 16, v82
	v_mul_f32_e32 v14, 0xbfb8aa3b, v12
	v_exp_f32_e32 v14, v14
	v_pk_mul_f32 v[86:87], v[6:7], v[86:87]
	v_add_f32_e32 v14, 1.0, v14
	v_pk_fma_f32 v[4:5], v[86:87], v[86:87], v[4:5]
	v_mul_f32_e32 v6, v87, v87
	v_pk_add_f32 v[4:5], v[6:7], v[4:5] op_sel_hi:[0,1]
	s_waitcnt lgkmcnt(1)
	v_lshlrev_b32_e32 v6, 16, v84
	v_and_b32_e32 v7, 0xffff0000, v84
	v_pk_fma_f32 v[0:1], v[70:71], v[6:7], v[0:1]
	v_mul_f32_e32 v6, 0xbfb8aa3b, v13
	v_exp_f32_e32 v6, v6
	v_rcp_f32_e32 v14, v14
	v_pk_mul_f32 v[0:1], v[0:1], v[12:13]
	v_and_b32_e32 v7, 0xffff0000, v83
	v_add_f32_e32 v6, 1.0, v6
	v_rcp_f32_e32 v15, v6
	v_lshlrev_b32_e32 v6, 16, v83
	v_mul_f32_e32 v12, 0xbfb8aa3b, v6
	v_exp_f32_e32 v12, v12
	v_pk_mul_f32 v[88:89], v[0:1], v[14:15]
	v_add_f32_e32 v12, 1.0, v12
	v_pk_fma_f32 v[0:1], v[88:89], v[88:89], v[4:5]
	v_mul_f32_e32 v4, v89, v89
	v_pk_add_f32 v[0:1], v[4:5], v[0:1] op_sel_hi:[0,1]
	v_lshlrev_b32_e32 v4, 16, v85
	v_and_b32_e32 v5, 0xffff0000, v85
	v_pk_fma_f32 v[2:3], v[70:71], v[4:5], v[2:3]
	v_mul_f32_e32 v4, 0xbfb8aa3b, v7
	v_exp_f32_e32 v4, v4
	v_rcp_f32_e32 v12, v12
	v_pk_mul_f32 v[2:3], v[2:3], v[6:7]
	s_waitcnt vmcnt(0)
	v_and_b32_e32 v5, 0xffff0000, v78
	v_add_f32_e32 v4, 1.0, v4
	v_rcp_f32_e32 v13, v4
	v_lshlrev_b32_e32 v4, 16, v78
	v_mul_f32_e32 v6, 0xbfb8aa3b, v4
	v_exp_f32_e32 v6, v6
	v_pk_mul_f32 v[82:83], v[2:3], v[12:13]
	v_add_f32_e32 v6, 1.0, v6
	v_pk_fma_f32 v[0:1], v[82:83], v[82:83], v[0:1]
	v_mul_f32_e32 v2, v83, v83
	v_pk_add_f32 v[0:1], v[2:3], v[0:1] op_sel_hi:[0,1]
	s_waitcnt lgkmcnt(0)
	v_lshlrev_b32_e32 v2, 16, v80
	v_and_b32_e32 v3, 0xffff0000, v80
	v_pk_fma_f32 v[2:3], v[70:71], v[2:3], v[8:9]
	v_rcp_f32_e32 v6, v6
	v_pk_mul_f32 v[2:3], v[2:3], v[4:5]
	v_mul_f32_e32 v4, 0xbfb8aa3b, v5
	v_exp_f32_e32 v4, v4
	v_and_b32_e32 v5, 0xffff0000, v79
	v_add_f32_e32 v4, 1.0, v4
	v_rcp_f32_e32 v7, v4
	v_lshlrev_b32_e32 v4, 16, v79
	v_pk_mul_f32 v[84:85], v[2:3], v[6:7]
	s_nop 0
	v_pk_fma_f32 v[0:1], v[84:85], v[84:85], v[0:1]
	v_mul_f32_e32 v2, v85, v85
	v_pk_add_f32 v[0:1], v[2:3], v[0:1] op_sel_hi:[0,1]
	v_lshlrev_b32_e32 v2, 16, v81
	v_and_b32_e32 v3, 0xffff0000, v81
	v_pk_fma_f32 v[2:3], v[70:71], v[2:3], v[10:11]
	v_mul_f32_e32 v6, 0xbfb8aa3b, v4
	v_pk_mul_f32 v[2:3], v[2:3], v[4:5]
	v_mul_f32_e32 v4, 0xbfb8aa3b, v5
	v_exp_f32_e32 v6, v6
	v_exp_f32_e32 v4, v4
	v_add_f32_e32 v6, 1.0, v6
	v_add_f32_e32 v4, 1.0, v4
	v_rcp_f32_e32 v6, v6
	v_rcp_f32_e32 v7, v4
	s_nop 0
	v_pk_mul_f32 v[70:71], v[2:3], v[6:7]
	s_nop 0
	v_pk_fma_f32 v[0:1], v[70:71], v[70:71], v[0:1]
	v_mul_f32_e32 v2, v71, v71
	v_pk_add_f32 v[0:1], v[2:3], v[0:1] op_sel_hi:[0,1]
	v_mov_b32_e32 v1, v0
	s_nop 1
	v_permlane16_swap_b32_e32 v0, v1
	v_add_f32_e32 v0, v0, v1
	v_mov_b32_e32 v1, v0
	s_nop 1
	v_permlane32_swap_b32_e32 v0, v1
	s_and_saveexec_b64 s[0:1], s[42:43]
	s_cbranch_execz .LBB0_1237
	v_add_f32_e32 v0, v0, v1
	ds_write_b32 v32, v0 offset:192
	s_branch .LBB0_1237
